# diff-attention: in the last two K/V steps of a query block, waves whose 32 rows lie wholly before the step's keys skip QK, softmax, rescale and PV (all scores causally masked); bit-identical
# baseline (speedup 1.0000x reference)
.LBB0_1365:
	s_and_b32 s72, s83, 0xffffffc0
	v_subrev_u32_e32 v130, s72, v219
	v_add_u32_e32 v182, 0x80, v130
	v_cvt_f32_i32_e32 v130, v182
	v_mul_f32_e64 v146, -v190, v130
	s_and_b32 s98, s65, 0xff
	s_cmp_gt_u32 s98, 0x60
	s_cbranch_scc1 .Lmk_a2
	v_mov_b32_e32 v221, 1.0
	v_mov_b32_e32 v222, 0
	v_mov_b32_e32 v223, 0
	v_readlane_b32 s76, v254, 14
	v_readlane_b32 s77, v254, 15
	v_readlane_b32 s83, v254, 16
	v_readlane_b32 s85, v254, 35
	s_mov_b32 s82, 0xf800000
	s_movk_i32 s84, 0x2200
	s_nop 4
	s_branch .Lmk_a2e
.Lmk_a2:
	s_mov_b32 s2, 0x41900000
	s_mov_b32 s3, 0x41980000
	v_pk_fma_f32 v[140:141], v[196:197], s[2:3], v[146:147] op_sel_hi:[1,1,0]
	s_mov_b32 s2, 0x41c00000
	s_mov_b32 s3, 0x41c80000
	v_pk_fma_f32 v[142:143], v[196:197], s[2:3], v[146:147] op_sel_hi:[1,1,0]
	s_mov_b32 s2, 0x41d00000
	s_mov_b32 s3, 0x41d80000
	v_pk_fma_f32 v[144:145], v[196:197], s[2:3], v[146:147] op_sel_hi:[1,1,0]
	s_mov_b32 s2, 0x42000000
	v_fma_f32 v131, -v190, v130, v190
	v_mov_b32_e32 v130, v146
	v_mov_b32_e32 v191, v190
	s_mov_b32 s3, 0x42040000
	v_fmac_f32_e32 v130, 0, v190
	v_pk_fma_f32 v[132:133], v[196:197], s[60:61], v[146:147] op_sel_hi:[1,1,0]
	v_pk_fma_f32 v[134:135], v[196:197], s[74:75], v[146:147] op_sel_hi:[1,1,0]
	v_pk_fma_f32 v[136:137], v[196:197], s[62:63], v[146:147] op_sel_hi:[1,1,0]
	v_pk_fma_f32 v[138:139], v[196:197], s[58:59], v[146:147] op_sel_hi:[1,1,0]
	v_pk_fma_f32 v[160:161], v[190:191], s[68:69], v[146:147] op_sel_hi:[1,1,0]
	v_pk_fma_f32 v[158:159], v[190:191], s[96:97], v[146:147] op_sel_hi:[1,1,0]
	v_pk_fma_f32 v[156:157], v[190:191], s[94:95], v[146:147] op_sel_hi:[1,1,0]
	v_pk_fma_f32 v[154:155], v[190:191], s[92:93], v[146:147] op_sel_hi:[1,1,0]
	v_pk_fma_f32 v[152:153], v[190:191], s[90:91], v[146:147] op_sel_hi:[1,1,0]
	v_pk_fma_f32 v[150:151], v[190:191], s[88:89], v[146:147] op_sel_hi:[1,1,0]
	v_pk_fma_f32 v[148:149], v[190:191], s[86:87], v[146:147] op_sel_hi:[1,1,0]
	v_pk_fma_f32 v[146:147], v[192:193], s[2:3], v[146:147] op_sel_hi:[1,1,0]
	s_setprio 1
	ds_read_b128 v[198:201], v205
	ds_read_b128 v[206:209], v205 offset:1024
	ds_read_b128 v[184:187], v224
	ds_read_b128 v[238:241], v224 offset:8192
	ds_read_b128 v[244:247], v223
	ds_read_b128 v[250:253], v223 offset:8192
	s_waitcnt lgkmcnt(3)
	v_mfma_f32_32x32x16_bf16 v[130:145], v[184:187], v[178:181], v[130:145]
	ds_read_b128 v[184:187], v222
	s_waitcnt lgkmcnt(3)
	v_mfma_f32_32x32x16_bf16 v[146:161], v[238:241], v[178:181], v[146:161]
	ds_read_b128 v[238:241], v222 offset:8192
	s_waitcnt lgkmcnt(3)
	v_mfma_f32_32x32x16_bf16 v[130:145], v[244:247], v[170:173], v[130:145]
	ds_read_b128 v[244:247], v221
	s_waitcnt lgkmcnt(3)
	v_mfma_f32_32x32x16_bf16 v[146:161], v[250:253], v[170:173], v[146:161]
	ds_read_b128 v[250:253], v221 offset:8192
	s_waitcnt lgkmcnt(3)
	v_mfma_f32_32x32x16_bf16 v[130:145], v[184:187], v[166:169], v[130:145]
	ds_read_b128 v[184:187], v224 offset:128
	s_waitcnt lgkmcnt(3)
	v_mfma_f32_32x32x16_bf16 v[146:161], v[238:241], v[166:169], v[146:161]
	ds_read_b128 v[238:241], v224 offset:8320
	s_waitcnt lgkmcnt(3)
	v_mfma_f32_32x32x16_bf16 v[130:145], v[244:247], v[162:165], v[130:145]
	ds_read_b128 v[244:247], v223 offset:128
	s_waitcnt lgkmcnt(3)
	v_mfma_f32_32x32x16_bf16 v[146:161], v[250:253], v[162:165], v[146:161]
	ds_read_b128 v[250:253], v223 offset:8320
	s_waitcnt lgkmcnt(3)
	v_mfma_f32_32x32x16_bf16 v[130:145], v[184:187], v[174:177], v[130:145]
	ds_read_b128 v[184:187], v222 offset:128
	s_waitcnt lgkmcnt(3)
	v_mfma_f32_32x32x16_bf16 v[146:161], v[238:241], v[174:177], v[146:161]
	ds_read_b128 v[238:241], v222 offset:8320
	s_waitcnt lgkmcnt(3)
	v_mfma_f32_32x32x16_bf16 v[130:145], v[244:247], v[198:201], v[130:145]
	ds_read_b128 v[244:247], v221 offset:128
	s_waitcnt lgkmcnt(3)
	v_mfma_f32_32x32x16_bf16 v[146:161], v[250:253], v[198:201], v[146:161]
	ds_read_b128 v[250:253], v221 offset:8320
	ds_read_b128 v[198:201], v205 offset:2048
	s_waitcnt lgkmcnt(4)
	v_mfma_f32_32x32x16_bf16 v[130:145], v[184:187], v[206:209], v[130:145]
	s_waitcnt lgkmcnt(3)
	v_mfma_f32_32x32x16_bf16 v[146:161], v[238:241], v[206:209], v[146:161]
	s_waitcnt lgkmcnt(0)
	v_mfma_f32_32x32x16_bf16 v[130:145], v[244:247], v[198:201], v[130:145]
	s_waitcnt lgkmcnt(0)
	v_mfma_f32_32x32x16_bf16 v[146:161], v[250:253], v[198:201], v[146:161]
	s_setprio 0
	s_add_i32 s2, s72, 0xffffffbf
	s_cmp_gt_i32 s2, s65
	s_cbranch_scc0 .LBB0_1367
	v_cmp_gt_i32_e64 s[60:61], 26, v182
	v_cmp_gt_i32_e64 s[62:63], 27, v182
	v_cmp_gt_i32_e64 s[58:59], 25, v182
	s_and_b64 s[60:61], s[62:63], s[60:61]
	v_cmp_gt_i32_e64 s[56:57], 24, v182
	s_and_b64 s[58:59], s[60:61], s[58:59]
	v_cmp_gt_i32_e64 s[54:55], 19, v182
	s_and_b64 s[56:57], s[58:59], s[56:57]
	v_cmp_gt_i32_e64 s[52:53], 18, v182
	s_and_b64 s[54:55], s[56:57], s[54:55]
	v_cmp_gt_i32_e64 s[50:51], 17, v182
	s_and_b64 s[52:53], s[54:55], s[52:53]
	v_cmp_gt_i32_e64 s[48:49], 16, v182
	s_and_b64 s[50:51], s[52:53], s[50:51]
	v_cmp_gt_i32_e64 s[46:47], 11, v182
	s_and_b64 s[48:49], s[50:51], s[48:49]
	v_cmp_gt_i32_e64 s[44:45], 10, v182
	s_and_b64 s[46:47], s[48:49], s[46:47]
	v_cmp_gt_i32_e64 s[42:43], 9, v182
	s_and_b64 s[44:45], s[46:47], s[44:45]
	v_cmp_gt_i32_e64 s[40:41], 8, v182
	s_and_b64 s[42:43], s[44:45], s[42:43]
	v_cmp_gt_i32_e64 s[38:39], 3, v182
	s_and_b64 s[40:41], s[42:43], s[40:41]
	v_cmp_gt_i32_e64 s[36:37], 2, v182
	s_and_b64 s[38:39], s[40:41], s[38:39]
	v_cmp_gt_i32_e64 s[34:35], 1, v182
	s_and_b64 s[36:37], s[38:39], s[36:37]
	v_cmp_gt_i32_e64 s[30:31], 0, v182
	s_and_b64 s[34:35], s[36:37], s[34:35]
	s_and_b64 s[30:31], s[34:35], s[30:31]
	v_cmp_gt_i32_e64 s[28:29], 58, v182
	v_cndmask_b32_e64 v130, v130, v243, s[30:31]
	v_cmp_gt_i32_e64 s[30:31], 59, v182
	v_cmp_gt_i32_e64 s[26:27], 57, v182
	s_and_b64 s[28:29], s[30:31], s[28:29]
	v_cmp_gt_i32_e64 s[24:25], 56, v182
	s_and_b64 s[26:27], s[28:29], s[26:27]
	v_cmp_gt_i32_e64 s[22:23], 51, v182
	s_and_b64 s[24:25], s[26:27], s[24:25]
	v_cmp_gt_i32_e64 s[20:21], 50, v182
	s_and_b64 s[22:23], s[24:25], s[22:23]
	v_cmp_gt_i32_e64 s[18:19], 49, v182
	s_and_b64 s[20:21], s[22:23], s[20:21]
	v_cmp_gt_i32_e64 s[16:17], 48, v182
	s_and_b64 s[18:19], s[20:21], s[18:19]
	v_cmp_gt_i32_e64 s[14:15], 43, v182
	s_and_b64 s[16:17], s[18:19], s[16:17]
	v_cmp_gt_i32_e64 s[12:13], 42, v182
	s_and_b64 s[14:15], s[16:17], s[14:15]
	v_cmp_gt_i32_e64 s[10:11], 41, v182
	s_and_b64 s[12:13], s[14:15], s[12:13]
	v_cmp_gt_i32_e64 s[8:9], 40, v182
	s_and_b64 s[10:11], s[12:13], s[10:11]
	v_cmp_gt_i32_e64 s[6:7], 35, v182
	s_and_b64 s[8:9], s[10:11], s[8:9]
	v_cmp_gt_i32_e64 s[4:5], 34, v182
	s_and_b64 s[6:7], s[8:9], s[6:7]
	v_cmp_gt_i32_e64 s[2:3], 33, v182
	s_and_b64 s[4:5], s[6:7], s[4:5]
	v_cmp_gt_i32_e32 vcc, 32, v182
	s_and_b64 s[2:3], s[4:5], s[2:3]
	v_cndmask_b32_e64 v145, v145, v243, s[62:63]
	s_mov_b32 s62, 0x41200000
	v_cndmask_b32_e64 v144, v144, v243, s[60:61]
	s_mov_b32 s60, 2.0
	v_cndmask_b32_e64 v143, v143, v243, s[58:59]
	s_mov_b32 s58, 0x41800000
	s_and_b64 vcc, s[2:3], vcc
	s_mov_b32 s63, 0x41300000
	s_mov_b32 s61, 0x40400000
	s_mov_b32 s59, 0x41880000
	v_cndmask_b32_e64 v142, v142, v243, s[56:57]
	v_cndmask_b32_e64 v141, v141, v243, s[54:55]
	v_cndmask_b32_e64 v140, v140, v243, s[52:53]
	v_cndmask_b32_e64 v139, v139, v243, s[50:51]
	v_cndmask_b32_e64 v138, v138, v243, s[48:49]
	v_cndmask_b32_e64 v137, v137, v243, s[46:47]
	v_cndmask_b32_e64 v136, v136, v243, s[44:45]
	v_cndmask_b32_e64 v135, v135, v243, s[42:43]
	v_cndmask_b32_e64 v134, v134, v243, s[40:41]
	v_cndmask_b32_e64 v133, v133, v243, s[38:39]
	v_cndmask_b32_e64 v132, v132, v243, s[36:37]
	v_cndmask_b32_e64 v131, v131, v243, s[34:35]
	v_cndmask_b32_e64 v161, v161, v243, s[30:31]
	v_cndmask_b32_e64 v160, v160, v243, s[28:29]
	v_cndmask_b32_e64 v159, v159, v243, s[26:27]
	v_cndmask_b32_e64 v158, v158, v243, s[24:25]
	v_cndmask_b32_e64 v157, v157, v243, s[22:23]
	v_cndmask_b32_e64 v156, v156, v243, s[20:21]
	v_cndmask_b32_e64 v155, v155, v243, s[18:19]
	v_cndmask_b32_e64 v154, v154, v243, s[16:17]
	v_cndmask_b32_e64 v153, v153, v243, s[14:15]
	v_cndmask_b32_e64 v152, v152, v243, s[12:13]
	v_cndmask_b32_e64 v151, v151, v243, s[10:11]
	v_cndmask_b32_e64 v150, v150, v243, s[8:9]
	v_cndmask_b32_e64 v149, v149, v243, s[6:7]
	v_cndmask_b32_e64 v148, v148, v243, s[4:5]
	v_cndmask_b32_e64 v147, v147, v243, s[2:3]
	v_cndmask_b32_e32 v146, v146, v243, vcc

.LBB0_1371:
.Lmk_a2e:
	s_mul_i32 s3, s72, 0x3100
	s_sub_i32 s2, s72, 64
	s_add_i32 s7, s3, 0xfff3c000
	s_mul_hi_u32 s6, s2, 0x3100
	s_add_u32 s4, s80, s7
	s_addc_u32 s5, s81, s6
	v_lshl_add_u64 v[150:151], s[4:5], 0, v[194:195]
	s_sub_i32 s4, s72, 32
	s_add_i32 s3, s3, 0xfff9e000
	s_mul_hi_u32 s8, s4, 0x3100
	s_add_u32 s4, s80, s3
	s_addc_u32 s5, s81, s8
	v_lshl_add_u64 v[154:155], s[4:5], 0, v[194:195]
	s_add_u32 s4, s78, s7
	s_addc_u32 s5, s79, s6
	v_lshl_add_u64 v[182:183], s[4:5], 0, v[194:195]
	s_add_u32 s4, s78, s3
	global_load_dwordx4 v[146:149], v[150:151], off
	s_nop 0
	global_load_dwordx4 v[150:153], v[150:151], off offset:256
	s_nop 0
	global_load_dwordx4 v[158:161], v[154:155], off
	s_nop 0
	global_load_dwordx4 v[154:157], v[154:155], off offset:256
	s_addc_u32 s5, s79, s8
	v_lshl_add_u64 v[186:187], s[4:5], 0, v[194:195]
	global_load_dwordx4 v[182:185], v[182:183], off
	s_nop 0
	global_load_dwordx4 v[186:189], v[186:187], off
	s_cmp_le_u32 s98, 0x60
	s_cbranch_scc1 .Lmk_b2e
	s_setprio 1
	ds_read_b64_tr_b16 v[206:207], v213 offset:0
	ds_read_b64_tr_b16 v[208:209], v213 offset:0x1000
	ds_read_b64_tr_b16 v[238:239], v213 offset:0x2000
	ds_read_b64_tr_b16 v[240:241], v213 offset:0x3000
	ds_read_b64_tr_b16 v[244:245], v213 offset:0x4000
	ds_read_b64_tr_b16 v[246:247], v213 offset:0x5000
	ds_read_b64_tr_b16 v[250:251], v213 offset:0x6000
	ds_read_b64_tr_b16 v[252:253], v213 offset:0x7000
	s_waitcnt lgkmcnt(0)
	s_nop 0
	v_mfma_f32_32x32x16_bf16 v[114:129], v[130:133], v[206:209], v[114:129]
	ds_read_b64_tr_b16 v[206:207], v213 offset:0x200
	ds_read_b64_tr_b16 v[208:209], v213 offset:0x1200
	v_mfma_f32_32x32x16_bf16 v[114:129], v[134:137], v[238:241], v[114:129]
	ds_read_b64_tr_b16 v[238:239], v213 offset:0x2200
	ds_read_b64_tr_b16 v[240:241], v213 offset:0x3200
	v_mfma_f32_32x32x16_bf16 v[114:129], v[138:141], v[244:247], v[114:129]
	ds_read_b64_tr_b16 v[244:245], v213 offset:0x4200
	ds_read_b64_tr_b16 v[246:247], v213 offset:0x5200
	v_mfma_f32_32x32x16_bf16 v[114:129], v[142:145], v[250:253], v[114:129]
	ds_read_b64_tr_b16 v[250:251], v213 offset:0x6200
	ds_read_b64_tr_b16 v[252:253], v213 offset:0x7200
	s_waitcnt lgkmcnt(0)
	v_mfma_f32_32x32x16_bf16 v[98:113], v[130:133], v[206:209], v[98:113]
	ds_read_b64_tr_b16 v[206:207], v213 offset:0x400
	ds_read_b64_tr_b16 v[208:209], v213 offset:0x1400
	v_mfma_f32_32x32x16_bf16 v[98:113], v[134:137], v[238:241], v[98:113]
	ds_read_b64_tr_b16 v[238:239], v213 offset:0x2400
	ds_read_b64_tr_b16 v[240:241], v213 offset:0x3400
	v_mfma_f32_32x32x16_bf16 v[98:113], v[138:141], v[244:247], v[98:113]
	ds_read_b64_tr_b16 v[244:245], v213 offset:0x4400
	ds_read_b64_tr_b16 v[246:247], v213 offset:0x5400
	v_mfma_f32_32x32x16_bf16 v[98:113], v[142:145], v[250:253], v[98:113]
	ds_read_b64_tr_b16 v[250:251], v213 offset:0x6400
	ds_read_b64_tr_b16 v[252:253], v213 offset:0x7400
	s_waitcnt lgkmcnt(0)
	v_mfma_f32_32x32x16_bf16 v[82:97], v[130:133], v[206:209], v[82:97]
	ds_read_b64_tr_b16 v[206:207], v213 offset:0x600
	ds_read_b64_tr_b16 v[208:209], v213 offset:0x1600
	v_mfma_f32_32x32x16_bf16 v[82:97], v[134:137], v[238:241], v[82:97]
	ds_read_b64_tr_b16 v[238:239], v213 offset:0x2600
	ds_read_b64_tr_b16 v[240:241], v213 offset:0x3600
	v_mfma_f32_32x32x16_bf16 v[82:97], v[138:141], v[244:247], v[82:97]
	ds_read_b64_tr_b16 v[244:245], v213 offset:0x4600
	ds_read_b64_tr_b16 v[246:247], v213 offset:0x5600
	v_mfma_f32_32x32x16_bf16 v[82:97], v[142:145], v[250:253], v[82:97]
	ds_read_b64_tr_b16 v[250:251], v213 offset:0x6600
	ds_read_b64_tr_b16 v[252:253], v213 offset:0x7600
	s_waitcnt lgkmcnt(0)
	v_mfma_f32_32x32x16_bf16 v[66:81], v[130:133], v[206:209], v[66:81]
	ds_read_b64_tr_b16 v[206:207], v213 offset:0x800
	ds_read_b64_tr_b16 v[208:209], v213 offset:0x1800
	v_mfma_f32_32x32x16_bf16 v[66:81], v[134:137], v[238:241], v[66:81]
	ds_read_b64_tr_b16 v[238:239], v213 offset:0x2800
	ds_read_b64_tr_b16 v[240:241], v213 offset:0x3800
	v_mfma_f32_32x32x16_bf16 v[66:81], v[138:141], v[244:247], v[66:81]
	ds_read_b64_tr_b16 v[244:245], v213 offset:0x4800
	ds_read_b64_tr_b16 v[246:247], v213 offset:0x5800
	v_mfma_f32_32x32x16_bf16 v[66:81], v[142:145], v[250:253], v[66:81]
	ds_read_b64_tr_b16 v[250:251], v213 offset:0x6800
	ds_read_b64_tr_b16 v[252:253], v213 offset:0x7800
	s_waitcnt lgkmcnt(0)
	v_mfma_f32_32x32x16_bf16 v[50:65], v[130:133], v[206:209], v[50:65]
	ds_read_b64_tr_b16 v[206:207], v213 offset:0xa00
	ds_read_b64_tr_b16 v[208:209], v213 offset:0x1a00
	v_mfma_f32_32x32x16_bf16 v[50:65], v[134:137], v[238:241], v[50:65]
	ds_read_b64_tr_b16 v[238:239], v213 offset:0x2a00
	ds_read_b64_tr_b16 v[240:241], v213 offset:0x3a00
	v_mfma_f32_32x32x16_bf16 v[50:65], v[138:141], v[244:247], v[50:65]
	ds_read_b64_tr_b16 v[244:245], v213 offset:0x4a00
	ds_read_b64_tr_b16 v[246:247], v213 offset:0x5a00
	v_mfma_f32_32x32x16_bf16 v[50:65], v[142:145], v[250:253], v[50:65]
	ds_read_b64_tr_b16 v[250:251], v213 offset:0x6a00
	ds_read_b64_tr_b16 v[252:253], v213 offset:0x7a00
	s_waitcnt lgkmcnt(0)
	v_mfma_f32_32x32x16_bf16 v[34:49], v[130:133], v[206:209], v[34:49]
	ds_read_b64_tr_b16 v[206:207], v213 offset:0xc00
	ds_read_b64_tr_b16 v[208:209], v213 offset:0x1c00
	v_mfma_f32_32x32x16_bf16 v[34:49], v[134:137], v[238:241], v[34:49]
	ds_read_b64_tr_b16 v[238:239], v213 offset:0x2c00
	ds_read_b64_tr_b16 v[240:241], v213 offset:0x3c00
	v_mfma_f32_32x32x16_bf16 v[34:49], v[138:141], v[244:247], v[34:49]
	ds_read_b64_tr_b16 v[244:245], v213 offset:0x4c00
	ds_read_b64_tr_b16 v[246:247], v213 offset:0x5c00
	v_mfma_f32_32x32x16_bf16 v[34:49], v[142:145], v[250:253], v[34:49]
	ds_read_b64_tr_b16 v[250:251], v213 offset:0x6c00
	ds_read_b64_tr_b16 v[252:253], v213 offset:0x7c00
	s_waitcnt lgkmcnt(0)
	v_mfma_f32_32x32x16_bf16 v[18:33], v[130:133], v[206:209], v[18:33]
	ds_read_b64_tr_b16 v[206:207], v213 offset:0xe00
	ds_read_b64_tr_b16 v[208:209], v213 offset:0x1e00
	v_mfma_f32_32x32x16_bf16 v[18:33], v[134:137], v[238:241], v[18:33]
	ds_read_b64_tr_b16 v[238:239], v213 offset:0x2e00
	ds_read_b64_tr_b16 v[240:241], v213 offset:0x3e00
	v_mfma_f32_32x32x16_bf16 v[18:33], v[138:141], v[244:247], v[18:33]
	ds_read_b64_tr_b16 v[244:245], v213 offset:0x4e00
	ds_read_b64_tr_b16 v[246:247], v213 offset:0x5e00
	v_mfma_f32_32x32x16_bf16 v[18:33], v[142:145], v[250:253], v[18:33]
	ds_read_b64_tr_b16 v[250:251], v213 offset:0x6e00
	ds_read_b64_tr_b16 v[252:253], v213 offset:0x7e00
	s_waitcnt lgkmcnt(0)
	v_mfma_f32_32x32x16_bf16 v[2:17], v[130:133], v[206:209], v[2:17]
	v_mfma_f32_32x32x16_bf16 v[2:17], v[134:137], v[238:241], v[2:17]
	v_mfma_f32_32x32x16_bf16 v[2:17], v[138:141], v[244:247], v[2:17]
	v_mfma_f32_32x32x16_bf16 v[2:17], v[142:145], v[250:253], v[2:17]
	s_setprio 0
.Lmk_b2e:
	s_waitcnt vmcnt(0)
	s_waitcnt vmcnt(1)
	ds_write_b128 v227, v[182:185]
	s_waitcnt vmcnt(0)
	ds_write_b128 v227, v[186:189] offset:8192
	ds_write_b128 v220, v[146:149] offset:32768
	ds_write_b128 v220, v[158:161] offset:49152
	ds_write_b128 v220, v[150:153] offset:34816
	ds_write_b128 v220, v[154:157] offset:51200
	v_subrev_u32_e32 v182, s2, v219
	v_cvt_f32_i32_e32 v130, v182
	s_waitcnt lgkmcnt(0)
	s_barrier
	v_mul_f32_e64 v146, -v190, v130
	s_cmp_gt_u32 s98, 0xa0
	s_cbranch_scc1 .Lmk_a1
	v_mov_b32_e32 v215, 1.0
	v_mov_b32_e32 v216, 0
	v_mov_b32_e32 v217, 0
	v_readlane_b32 s28, v254, 56
	v_readlane_b32 s56, v254, 33
	v_readlane_b32 s29, v254, 57
	v_readlane_b32 s6, v254, 48
	v_readlane_b32 s7, v254, 19
	v_readlane_b32 s12, v254, 21
	v_readlane_b32 s57, v254, 34
	s_mov_b64 s[52:53], 0x400
	s_nop 4
	s_branch .Lmk_a1e
.Lmk_a1:
	s_mov_b32 s2, 0x41900000
	s_mov_b32 s3, 0x41980000
	v_pk_fma_f32 v[140:141], v[196:197], s[2:3], v[146:147] op_sel_hi:[1,1,0]
	s_mov_b32 s2, 0x41c00000
	s_mov_b32 s3, 0x41c80000
	v_pk_fma_f32 v[142:143], v[196:197], s[2:3], v[146:147] op_sel_hi:[1,1,0]
	s_mov_b32 s2, 0x41d00000
	s_mov_b32 s3, 0x41d80000
	v_pk_fma_f32 v[144:145], v[196:197], s[2:3], v[146:147] op_sel_hi:[1,1,0]
	s_mov_b32 s2, 0x42000000
	v_fma_f32 v131, -v190, v130, v190
	v_mov_b32_e32 v130, v146
	v_mov_b32_e32 v191, v190
	s_mov_b32 s3, 0x42040000
	v_fmac_f32_e32 v130, 0, v190
	v_pk_fma_f32 v[132:133], v[196:197], s[60:61], v[146:147] op_sel_hi:[1,1,0]
	v_pk_fma_f32 v[134:135], v[196:197], s[74:75], v[146:147] op_sel_hi:[1,1,0]
	v_pk_fma_f32 v[136:137], v[196:197], s[62:63], v[146:147] op_sel_hi:[1,1,0]
	v_pk_fma_f32 v[138:139], v[196:197], s[58:59], v[146:147] op_sel_hi:[1,1,0]
	v_pk_fma_f32 v[160:161], v[190:191], s[68:69], v[146:147] op_sel_hi:[1,1,0]
	v_pk_fma_f32 v[158:159], v[190:191], s[96:97], v[146:147] op_sel_hi:[1,1,0]
	v_pk_fma_f32 v[156:157], v[190:191], s[94:95], v[146:147] op_sel_hi:[1,1,0]
	v_pk_fma_f32 v[154:155], v[190:191], s[92:93], v[146:147] op_sel_hi:[1,1,0]
	v_pk_fma_f32 v[152:153], v[190:191], s[90:91], v[146:147] op_sel_hi:[1,1,0]
	v_pk_fma_f32 v[150:151], v[190:191], s[88:89], v[146:147] op_sel_hi:[1,1,0]
	v_pk_fma_f32 v[148:149], v[190:191], s[86:87], v[146:147] op_sel_hi:[1,1,0]
	v_pk_fma_f32 v[146:147], v[192:193], s[2:3], v[146:147] op_sel_hi:[1,1,0]
	s_setprio 1
	ds_read_b128 v[184:187], v218
	s_waitcnt lgkmcnt(0)
	v_mfma_f32_32x32x16_bf16 v[130:145], v[184:187], v[178:181], v[130:145]
	ds_read_b128 v[184:187], v218 offset:8192
	s_waitcnt lgkmcnt(0)
	v_mfma_f32_32x32x16_bf16 v[146:161], v[184:187], v[178:181], v[146:161]
	ds_read_b128 v[178:181], v217
	s_waitcnt lgkmcnt(0)
	v_mfma_f32_32x32x16_bf16 v[130:145], v[178:181], v[170:173], v[130:145]
	ds_read_b128 v[178:181], v217 offset:8192
	s_waitcnt lgkmcnt(0)
	v_mfma_f32_32x32x16_bf16 v[146:161], v[178:181], v[170:173], v[146:161]
	ds_read_b128 v[170:173], v216
	s_waitcnt lgkmcnt(0)
	v_mfma_f32_32x32x16_bf16 v[130:145], v[170:173], v[166:169], v[130:145]
	ds_read_b128 v[170:173], v216 offset:8192
	s_waitcnt lgkmcnt(0)
	v_mfma_f32_32x32x16_bf16 v[146:161], v[170:173], v[166:169], v[146:161]
	ds_read_b128 v[166:169], v215
	s_waitcnt lgkmcnt(0)
	v_mfma_f32_32x32x16_bf16 v[130:145], v[166:169], v[162:165], v[130:145]
	ds_read_b128 v[166:169], v215 offset:8192
	s_waitcnt lgkmcnt(0)
	v_mfma_f32_32x32x16_bf16 v[146:161], v[166:169], v[162:165], v[146:161]
	ds_read_b128 v[162:165], v218 offset:128
	s_waitcnt lgkmcnt(0)
	v_mfma_f32_32x32x16_bf16 v[130:145], v[162:165], v[174:177], v[130:145]
	ds_read_b128 v[162:165], v218 offset:8320
	s_waitcnt lgkmcnt(0)
	v_mfma_f32_32x32x16_bf16 v[146:161], v[162:165], v[174:177], v[146:161]
	ds_read_b128 v[162:165], v217 offset:128
	ds_read_b128 v[166:169], v205
	s_waitcnt lgkmcnt(0)
	v_mfma_f32_32x32x16_bf16 v[130:145], v[162:165], v[166:169], v[130:145]
	ds_read_b128 v[162:165], v217 offset:8320
	s_waitcnt lgkmcnt(0)
	v_mfma_f32_32x32x16_bf16 v[146:161], v[162:165], v[166:169], v[146:161]
	ds_read_b128 v[162:165], v216 offset:128
	ds_read_b128 v[166:169], v205 offset:1024
	s_waitcnt lgkmcnt(0)
	v_mfma_f32_32x32x16_bf16 v[130:145], v[162:165], v[166:169], v[130:145]
	ds_read_b128 v[162:165], v216 offset:8320
	s_waitcnt lgkmcnt(0)
	v_mfma_f32_32x32x16_bf16 v[146:161], v[162:165], v[166:169], v[146:161]
	ds_read_b128 v[162:165], v215 offset:128
	ds_read_b128 v[166:169], v205 offset:2048
	s_waitcnt lgkmcnt(0)
	v_mfma_f32_32x32x16_bf16 v[130:145], v[162:165], v[166:169], v[130:145]
	ds_read_b128 v[162:165], v215 offset:8320
	s_waitcnt lgkmcnt(0)
	v_mfma_f32_32x32x16_bf16 v[146:161], v[162:165], v[166:169], v[146:161]
	s_setprio 0
	s_add_i32 s72, s72, -1
	s_cmp_le_i32 s72, s65
	s_cbranch_scc1 .LBB0_1373
	v_cmp_gt_i32_e64 s[60:61], 26, v182
	v_cmp_gt_i32_e64 s[62:63], 27, v182
	v_cmp_gt_i32_e64 s[58:59], 25, v182
	s_and_b64 s[60:61], s[62:63], s[60:61]
	v_cmp_gt_i32_e64 s[56:57], 24, v182
	s_and_b64 s[58:59], s[60:61], s[58:59]
	v_cmp_gt_i32_e64 s[54:55], 19, v182
	s_and_b64 s[56:57], s[58:59], s[56:57]
	v_cmp_gt_i32_e64 s[52:53], 18, v182
	s_and_b64 s[54:55], s[56:57], s[54:55]
	v_cmp_gt_i32_e64 s[50:51], 17, v182
	s_and_b64 s[52:53], s[54:55], s[52:53]
	v_cmp_gt_i32_e64 s[48:49], 16, v182
	s_and_b64 s[50:51], s[52:53], s[50:51]
	v_cmp_gt_i32_e64 s[46:47], 11, v182
	s_and_b64 s[48:49], s[50:51], s[48:49]
	v_cmp_gt_i32_e64 s[44:45], 10, v182
	s_and_b64 s[46:47], s[48:49], s[46:47]
	v_cmp_gt_i32_e64 s[42:43], 9, v182
	s_and_b64 s[44:45], s[46:47], s[44:45]
	v_cmp_gt_i32_e64 s[40:41], 8, v182
	s_and_b64 s[42:43], s[44:45], s[42:43]
	v_cmp_gt_i32_e64 s[38:39], 3, v182
	s_and_b64 s[40:41], s[42:43], s[40:41]
	v_cmp_gt_i32_e64 s[36:37], 2, v182
	s_and_b64 s[38:39], s[40:41], s[38:39]
	v_cmp_gt_i32_e64 s[34:35], 1, v182
	s_and_b64 s[36:37], s[38:39], s[36:37]
	v_cmp_gt_i32_e64 s[30:31], 0, v182
	s_and_b64 s[34:35], s[36:37], s[34:35]
	s_and_b64 s[30:31], s[34:35], s[30:31]
	v_cmp_gt_i32_e64 s[28:29], 58, v182
	v_cndmask_b32_e64 v130, v130, v243, s[30:31]
	v_cmp_gt_i32_e64 s[30:31], 59, v182
	v_cmp_gt_i32_e64 s[26:27], 57, v182
	s_and_b64 s[28:29], s[30:31], s[28:29]
	v_cmp_gt_i32_e64 s[24:25], 56, v182
	s_and_b64 s[26:27], s[28:29], s[26:27]
	v_cmp_gt_i32_e64 s[22:23], 51, v182
	s_and_b64 s[24:25], s[26:27], s[24:25]
	v_cmp_gt_i32_e64 s[20:21], 50, v182
	s_and_b64 s[22:23], s[24:25], s[22:23]
	v_cmp_gt_i32_e64 s[18:19], 49, v182
	s_and_b64 s[20:21], s[22:23], s[20:21]
	v_cmp_gt_i32_e64 s[16:17], 48, v182
	s_and_b64 s[18:19], s[20:21], s[18:19]
	v_cmp_gt_i32_e64 s[14:15], 43, v182
	s_and_b64 s[16:17], s[18:19], s[16:17]
	v_cmp_gt_i32_e64 s[12:13], 42, v182
	s_and_b64 s[14:15], s[16:17], s[14:15]
	v_cmp_gt_i32_e64 s[10:11], 41, v182
	s_and_b64 s[12:13], s[14:15], s[12:13]
	v_cmp_gt_i32_e64 s[8:9], 40, v182
	s_and_b64 s[10:11], s[12:13], s[10:11]
	v_cmp_gt_i32_e64 s[6:7], 35, v182
	s_and_b64 s[8:9], s[10:11], s[8:9]
	v_cmp_gt_i32_e64 s[4:5], 34, v182
	s_and_b64 s[6:7], s[8:9], s[6:7]
	v_cmp_gt_i32_e64 s[2:3], 33, v182
	s_and_b64 s[4:5], s[6:7], s[4:5]
	v_cmp_gt_i32_e32 vcc, 32, v182
	s_and_b64 s[2:3], s[4:5], s[2:3]
	v_cndmask_b32_e64 v145, v145, v243, s[62:63]
	s_mov_b32 s62, 0x41200000
	v_cndmask_b32_e64 v144, v144, v243, s[60:61]
	s_mov_b32 s60, 2.0
	v_cndmask_b32_e64 v143, v143, v243, s[58:59]
	s_mov_b32 s58, 0x41800000
	s_and_b64 vcc, s[2:3], vcc
	s_mov_b32 s63, 0x41300000
	s_mov_b32 s61, 0x40400000
	s_mov_b32 s59, 0x41880000
	v_cndmask_b32_e64 v142, v142, v243, s[56:57]
	v_cndmask_b32_e64 v141, v141, v243, s[54:55]
	v_cndmask_b32_e64 v140, v140, v243, s[52:53]
	v_cndmask_b32_e64 v139, v139, v243, s[50:51]
	v_cndmask_b32_e64 v138, v138, v243, s[48:49]
	v_cndmask_b32_e64 v137, v137, v243, s[46:47]
	v_cndmask_b32_e64 v136, v136, v243, s[44:45]
	v_cndmask_b32_e64 v135, v135, v243, s[42:43]
	v_cndmask_b32_e64 v134, v134, v243, s[40:41]
	v_cndmask_b32_e64 v133, v133, v243, s[38:39]
	v_cndmask_b32_e64 v132, v132, v243, s[36:37]
	v_cndmask_b32_e64 v131, v131, v243, s[34:35]
	v_cndmask_b32_e64 v161, v161, v243, s[30:31]
	v_cndmask_b32_e64 v160, v160, v243, s[28:29]
	v_cndmask_b32_e64 v159, v159, v243, s[26:27]
	v_cndmask_b32_e64 v158, v158, v243, s[24:25]
	v_cndmask_b32_e64 v157, v157, v243, s[22:23]
	v_cndmask_b32_e64 v156, v156, v243, s[20:21]
	v_cndmask_b32_e64 v155, v155, v243, s[18:19]
	v_cndmask_b32_e64 v154, v154, v243, s[16:17]
	v_cndmask_b32_e64 v153, v153, v243, s[14:15]
	v_cndmask_b32_e64 v152, v152, v243, s[12:13]
	v_cndmask_b32_e64 v151, v151, v243, s[10:11]
	v_cndmask_b32_e64 v150, v150, v243, s[8:9]
	v_cndmask_b32_e64 v149, v149, v243, s[6:7]
	v_cndmask_b32_e64 v148, v148, v243, s[4:5]
	v_cndmask_b32_e64 v147, v147, v243, s[2:3]
	v_cndmask_b32_e32 v146, v146, v243, vcc

.LBB0_1377:
.Lmk_a1e:
	v_readlane_b32 s2, v254, 29
	v_readlane_b32 s3, v254, 30
	s_nop 1
	v_lshl_add_u64 v[130:131], s[2:3], 0, v[194:195]
	v_readlane_b32 s2, v254, 39
	v_add_co_u32_e32 v132, vcc, 0x62000, v130
	v_readlane_b32 s3, v254, 40
	s_nop 0
	v_addc_co_u32_e32 v133, vcc, 0, v131, vcc
	global_load_dwordx4 v[142:145], v[130:131], off
	global_load_dwordx4 v[146:149], v[130:131], off offset:256
	global_load_dwordx4 v[154:157], v[132:133], off
	global_load_dwordx4 v[150:153], v[132:133], off offset:256
	v_lshl_add_u64 v[130:131], s[2:3], 0, v[194:195]
	v_add_co_u32_e32 v132, vcc, 0x62000, v130
	s_nop 1
	v_addc_co_u32_e32 v133, vcc, 0, v131, vcc
	global_load_dwordx4 v[194:197], v[130:131], off
	global_load_dwordx4 v[198:201], v[132:133], off
	v_readlane_b32 s2, v254, 25
	v_readlane_b32 s3, v254, 26
	v_or_b32_e32 v132, s64, v242
	v_mov_b32_e32 v205, v1
	v_mov_b64_e32 v[130:131], s[2:3]
	v_mad_i64_i32 v[130:131], s[2:3], v132, s71, v[130:131]
	v_lshl_add_u64 v[138:139], v[130:131], 0, v[204:205]
	global_load_dwordx4 v[178:181], v[138:139], off
	global_load_dwordx4 v[170:173], v[138:139], off offset:32
	global_load_dwordx4 v[166:169], v[138:139], off offset:64
	global_load_dwordx4 v[162:165], v[138:139], off offset:96
	global_load_dwordx4 v[174:177], v[138:139], off offset:128
	global_load_dwordx4 v[130:133], v[138:139], off offset:160
	global_load_dwordx4 v[134:137], v[138:139], off offset:192
	s_nop 0
	global_load_dwordx4 v[138:141], v[138:139], off offset:224
	s_cmp_le_u32 s98, 0xa0
	s_cbranch_scc1 .Lmk_b1e
	s_setprio 1
	ds_read_b64_tr_b16 v[204:205], v213 offset:0x8000
	ds_read_b64_tr_b16 v[206:207], v213 offset:0x9000
	ds_read_b64_tr_b16 v[224:225], v213 offset:0xa000
	ds_read_b64_tr_b16 v[226:227], v213 offset:0xb000
	ds_read_b64_tr_b16 v[238:239], v213 offset:0xc000
	ds_read_b64_tr_b16 v[240:241], v213 offset:0xd000
	ds_read_b64_tr_b16 v[244:245], v213 offset:0xe000
	ds_read_b64_tr_b16 v[246:247], v213 offset:0xf000
	s_waitcnt lgkmcnt(0)
	s_nop 0
	v_mfma_f32_32x32x16_bf16 v[114:129], v[158:161], v[204:207], v[114:129]
	ds_read_b64_tr_b16 v[204:205], v213 offset:0x8200
	ds_read_b64_tr_b16 v[206:207], v213 offset:0x9200
	v_mfma_f32_32x32x16_bf16 v[114:129], v[182:185], v[224:227], v[114:129]
	ds_read_b64_tr_b16 v[224:225], v213 offset:0xa200
	ds_read_b64_tr_b16 v[226:227], v213 offset:0xb200
	v_mfma_f32_32x32x16_bf16 v[114:129], v[186:189], v[238:241], v[114:129]
	ds_read_b64_tr_b16 v[238:239], v213 offset:0xc200
	ds_read_b64_tr_b16 v[240:241], v213 offset:0xd200
	v_mfma_f32_32x32x16_bf16 v[114:129], v[190:193], v[244:247], v[114:129]
	ds_read_b64_tr_b16 v[244:245], v213 offset:0xe200
	ds_read_b64_tr_b16 v[246:247], v213 offset:0xf200
	s_waitcnt lgkmcnt(0)
	v_mfma_f32_32x32x16_bf16 v[98:113], v[158:161], v[204:207], v[98:113]
	ds_read_b64_tr_b16 v[204:205], v213 offset:0x8400
	ds_read_b64_tr_b16 v[206:207], v213 offset:0x9400
	v_mfma_f32_32x32x16_bf16 v[98:113], v[182:185], v[224:227], v[98:113]
	ds_read_b64_tr_b16 v[224:225], v213 offset:0xa400
	ds_read_b64_tr_b16 v[226:227], v213 offset:0xb400
	v_mfma_f32_32x32x16_bf16 v[98:113], v[186:189], v[238:241], v[98:113]
	ds_read_b64_tr_b16 v[238:239], v213 offset:0xc400
	ds_read_b64_tr_b16 v[240:241], v213 offset:0xd400
	v_mfma_f32_32x32x16_bf16 v[98:113], v[190:193], v[244:247], v[98:113]
	ds_read_b64_tr_b16 v[244:245], v213 offset:0xe400
	ds_read_b64_tr_b16 v[246:247], v213 offset:0xf400
	s_waitcnt lgkmcnt(0)
	v_mfma_f32_32x32x16_bf16 v[82:97], v[158:161], v[204:207], v[82:97]
	ds_read_b64_tr_b16 v[204:205], v213 offset:0x8600
	ds_read_b64_tr_b16 v[206:207], v213 offset:0x9600
	v_mfma_f32_32x32x16_bf16 v[82:97], v[182:185], v[224:227], v[82:97]
	ds_read_b64_tr_b16 v[224:225], v213 offset:0xa600
	ds_read_b64_tr_b16 v[226:227], v213 offset:0xb600
	v_mfma_f32_32x32x16_bf16 v[82:97], v[186:189], v[238:241], v[82:97]
	ds_read_b64_tr_b16 v[238:239], v213 offset:0xc600
	ds_read_b64_tr_b16 v[240:241], v213 offset:0xd600
	v_mfma_f32_32x32x16_bf16 v[82:97], v[190:193], v[244:247], v[82:97]
	ds_read_b64_tr_b16 v[244:245], v213 offset:0xe600
	ds_read_b64_tr_b16 v[246:247], v213 offset:0xf600
	s_waitcnt lgkmcnt(0)
	v_mfma_f32_32x32x16_bf16 v[66:81], v[158:161], v[204:207], v[66:81]
	ds_read_b64_tr_b16 v[204:205], v213 offset:0x8800
	ds_read_b64_tr_b16 v[206:207], v213 offset:0x9800
	v_mfma_f32_32x32x16_bf16 v[66:81], v[182:185], v[224:227], v[66:81]
	ds_read_b64_tr_b16 v[224:225], v213 offset:0xa800
	ds_read_b64_tr_b16 v[226:227], v213 offset:0xb800
	v_mfma_f32_32x32x16_bf16 v[66:81], v[186:189], v[238:241], v[66:81]
	ds_read_b64_tr_b16 v[238:239], v213 offset:0xc800
	ds_read_b64_tr_b16 v[240:241], v213 offset:0xd800
	v_mfma_f32_32x32x16_bf16 v[66:81], v[190:193], v[244:247], v[66:81]
	ds_read_b64_tr_b16 v[244:245], v213 offset:0xe800
	ds_read_b64_tr_b16 v[246:247], v213 offset:0xf800
	s_waitcnt lgkmcnt(0)
	v_mfma_f32_32x32x16_bf16 v[50:65], v[158:161], v[204:207], v[50:65]
	ds_read_b64_tr_b16 v[204:205], v213 offset:0x8a00
	ds_read_b64_tr_b16 v[206:207], v213 offset:0x9a00
	v_mfma_f32_32x32x16_bf16 v[50:65], v[182:185], v[224:227], v[50:65]
	ds_read_b64_tr_b16 v[224:225], v213 offset:0xaa00
	ds_read_b64_tr_b16 v[226:227], v213 offset:0xba00
	v_mfma_f32_32x32x16_bf16 v[50:65], v[186:189], v[238:241], v[50:65]
	ds_read_b64_tr_b16 v[238:239], v213 offset:0xca00
	ds_read_b64_tr_b16 v[240:241], v213 offset:0xda00
	v_mfma_f32_32x32x16_bf16 v[50:65], v[190:193], v[244:247], v[50:65]
	ds_read_b64_tr_b16 v[244:245], v213 offset:0xea00
	ds_read_b64_tr_b16 v[246:247], v213 offset:0xfa00
	s_waitcnt lgkmcnt(0)
	v_mfma_f32_32x32x16_bf16 v[34:49], v[158:161], v[204:207], v[34:49]
	ds_read_b64_tr_b16 v[204:205], v213 offset:0x8c00
	ds_read_b64_tr_b16 v[206:207], v213 offset:0x9c00
	v_mfma_f32_32x32x16_bf16 v[34:49], v[182:185], v[224:227], v[34:49]
	ds_read_b64_tr_b16 v[224:225], v213 offset:0xac00
	ds_read_b64_tr_b16 v[226:227], v213 offset:0xbc00
	v_mfma_f32_32x32x16_bf16 v[34:49], v[186:189], v[238:241], v[34:49]
	ds_read_b64_tr_b16 v[238:239], v213 offset:0xcc00
	ds_read_b64_tr_b16 v[240:241], v213 offset:0xdc00
	v_mfma_f32_32x32x16_bf16 v[34:49], v[190:193], v[244:247], v[34:49]
	ds_read_b64_tr_b16 v[244:245], v213 offset:0xec00
	ds_read_b64_tr_b16 v[246:247], v213 offset:0xfc00
	s_waitcnt lgkmcnt(0)
	v_mfma_f32_32x32x16_bf16 v[18:33], v[158:161], v[204:207], v[18:33]
	ds_read_b64_tr_b16 v[204:205], v213 offset:0x8e00
	ds_read_b64_tr_b16 v[206:207], v213 offset:0x9e00
	v_mfma_f32_32x32x16_bf16 v[18:33], v[182:185], v[224:227], v[18:33]
	ds_read_b64_tr_b16 v[224:225], v213 offset:0xae00
	ds_read_b64_tr_b16 v[226:227], v213 offset:0xbe00
	v_mfma_f32_32x32x16_bf16 v[18:33], v[186:189], v[238:241], v[18:33]
	ds_read_b64_tr_b16 v[238:239], v213 offset:0xce00
	ds_read_b64_tr_b16 v[240:241], v213 offset:0xde00
	v_mfma_f32_32x32x16_bf16 v[18:33], v[190:193], v[244:247], v[18:33]
	ds_read_b64_tr_b16 v[244:245], v213 offset:0xee00
	ds_read_b64_tr_b16 v[246:247], v213 offset:0xfe00
	s_waitcnt lgkmcnt(0)
	v_mfma_f32_32x32x16_bf16 v[2:17], v[158:161], v[204:207], v[2:17]
	v_mfma_f32_32x32x16_bf16 v[2:17], v[182:185], v[224:227], v[2:17]
	v_mfma_f32_32x32x16_bf16 v[2:17], v[186:189], v[238:241], v[2:17]
	v_mfma_f32_32x32x16_bf16 v[2:17], v[190:193], v[244:247], v[2:17]
	s_setprio 0
.Lmk_b1e:
	s_waitcnt vmcnt(8)
	s_waitcnt vmcnt(9)
	ds_write_b128 v0, v[194:197]
	s_waitcnt vmcnt(8)
	ds_write_b128 v0, v[198:201] offset:8192
	s_and_saveexec_b64 s[2:3], s[0:1]
	v_add_f32_e32 v0, v222, v223
	v_fmac_f32_e32 v0, v214, v221
	v_add_f32_e32 v158, v216, v217
	v_fmac_f32_e32 v158, v0, v215
	ds_write_b32 v212, v158
	s_or_b64 exec, exec, s[2:3]
	s_waitcnt lgkmcnt(0)
	ds_read_b128 v[190:193], v211
	s_ashr_i32 s65, s64, 31
	ds_read_b128 v[186:189], v211 offset:32
	ds_read_b128 v[182:185], v211 offset:64
	ds_read_b128 v[158:161], v211 offset:96
	s_lshl_b64 s[0:1], s[64:65], 13
	v_readlane_b32 s2, v254, 17
	s_waitcnt lgkmcnt(3)
	v_rcp_f32_e32 v190, v190
	v_readlane_b32 s3, v254, 18
	s_add_u32 s2, s2, s0
	v_and_b32_e32 v0, 1, v233
	s_addc_u32 s3, s3, s1
	v_cmp_eq_u32_e64 s[0:1], 0, v0
	v_lshlrev_b32_e32 v0, 1, v242
	v_lshl_add_u64 v[194:195], s[2:3], 0, v[0:1]
	v_lshlrev_b32_e32 v0, 15, v210
	v_lshl_add_u64 v[194:195], v[194:195], 0, v[0:1]
	v_mul_f32_e32 v0, v114, v190
	s_nop 1
	v_mov_b32_dpp v114, v0 quad_perm:[1,0,3,2] row_mask:0xf bank_mask:0xf bound_ctrl:1
	s_and_saveexec_b64 s[2:3], s[0:1]
	s_cbranch_execz .LBB0_1381
	v_cvt_pk_bf16_f32 v0, v0, v114
	global_store_dword v[194:195], v0, off
